# speedup vs baseline: 1.0315x; 1.0028x over previous
_Z8gemm2b_kILi2EEvPKtS1_ii7EpiArgs:
	s_bitcmp1_b32 s2, 8
	s_cbranch_scc0 .Lup_nodelay
	s_sleep 20
.Lup_nodelay:
	s_load_dwordx4 s[4:7], s[0:1], 0x0
	s_load_dwordx2 s[12:13], s[0:1], 0x10
	s_lshl_b32 s3, s2, 3
	s_and_b32 s3, s3, 56
	s_bfe_u32 s8, s2, 0x30003
	s_or_b32 s3, s3, s8
	s_lshl_b32 s17, s3, 7
	v_readfirstlane_b32 s19, v0
	s_waitcnt lgkmcnt(0)
	s_mul_hi_i32 s9, s13, s17
	s_mul_i32 s8, s13, s17
	s_lshr_b32 s14, s19, 6
	s_lshr_b32 s2, s2, 6
	s_ashr_i32 s11, s13, 31
	s_lshl_b64 s[8:9], s[8:9], 1
	s_mulk_i32 s2, 0xc0
	s_add_u32 s4, s4, s8
	s_addc_u32 s5, s5, s9
	s_mul_hi_i32 s9, s13, s2
	s_mul_i32 s8, s13, s2
	s_ashr_i32 s3, s2, 31
	s_lshl_b64 s[8:9], s[8:9], 1
	s_add_u32 s6, s6, s8
	s_addc_u32 s7, s7, s9
	s_lshr_b32 s8, s19, 1
	v_lshrrev_b32_e32 v1, 4, v0
	s_lshl_b32 s21, s14, 10
	s_and_b32 s16, s8, 0x7fffffc0
	v_xor_b32_e32 v3, v1, v0
	s_bitcmp1_b32 s19, 6
	v_lshrrev_b32_e32 v2, 3, v0
	v_lshlrev_b32_e32 v3, 3, v3
	s_cselect_b32 s18, 0x60, 0
	s_cmp_lg_u32 0, -1
	v_mul_lo_u32 v2, s13, v2
	v_and_b32_e32 v3, 56, v3
	s_mov_b32 s10, s13
	s_cselect_b32 s8, 0, 0
	v_add_lshl_u32 v104, v2, v3, 1
	s_add_i32 s22, s21, s8
	s_nop 4
	s_mov_b32 s8, m0
	s_mov_b32 m0, s22
	s_nop 0
	global_load_lds_dwordx4 v104, s[4:5]
	s_mov_b32 m0, s8
	s_lshl_b64 s[14:15], s[10:11], 6
	s_add_u32 s8, s4, s14
	s_addc_u32 s9, s5, s15
	s_add_i32 s23, s22, 0x1000
	s_nop 4
	s_mov_b32 s24, m0
	s_mov_b32 m0, s23
	s_nop 0
	global_load_lds_dwordx4 v104, s[8:9]
	s_mov_b32 m0, s24
	s_add_u32 s8, s8, s14
	s_addc_u32 s9, s9, s15
	s_add_i32 s24, s22, 0x2000
	s_nop 4
	s_mov_b32 s25, m0
	s_mov_b32 m0, s24
	s_nop 0
	global_load_lds_dwordx4 v104, s[8:9]
	s_mov_b32 m0, s25
	s_add_u32 s8, s8, s14
	s_addc_u32 s9, s9, s15
	s_add_i32 s25, s22, 0x3000
	s_nop 4
	s_mov_b32 s26, m0
	s_mov_b32 m0, s25
	s_nop 0
	global_load_lds_dwordx4 v104, s[8:9]
	s_mov_b32 m0, s26
	s_add_i32 s26, s22, 0x4000
	s_nop 4
	s_mov_b32 s8, m0
	s_mov_b32 m0, s26
	s_nop 0
	global_load_lds_dwordx4 v104, s[6:7]
	s_mov_b32 m0, s8
	s_add_u32 s8, s6, s14
	s_addc_u32 s9, s7, s15
	s_add_i32 s27, s22, 0x5000
	s_nop 4
	s_mov_b32 s28, m0
	s_mov_b32 m0, s27
	s_nop 0
	global_load_lds_dwordx4 v104, s[8:9]
	s_mov_b32 m0, s28
	s_add_u32 s8, s8, s14
	s_addc_u32 s9, s9, s15
	s_add_i32 s28, s22, 0x6000
	s_nop 4
	s_mov_b32 s29, m0
	s_mov_b32 m0, s28
	s_nop 0
	global_load_lds_dwordx4 v104, s[8:9]
	s_mov_b32 m0, s29
	s_add_u32 s8, s8, s14
	s_addc_u32 s9, s9, s15
	s_add_i32 s29, s22, 0x7000
	s_nop 4
	s_mov_b32 s30, m0
	s_mov_b32 m0, s29
	s_nop 0
	global_load_lds_dwordx4 v104, s[8:9]
	s_mov_b32 m0, s30
	s_add_u32 s8, s8, s14
	s_addc_u32 s9, s9, s15
	s_add_i32 s30, s22, 0x8000
	s_nop 4
	s_mov_b32 s31, m0
	s_mov_b32 m0, s30
	s_nop 0
	global_load_lds_dwordx4 v104, s[8:9]
	s_mov_b32 m0, s31
	s_add_u32 s8, s8, s14
	s_addc_u32 s9, s9, s15
	s_add_i32 s31, s22, 0x9000
	s_nop 4
	s_mov_b32 s33, m0
	s_mov_b32 m0, s31
	s_nop 0
	global_load_lds_dwordx4 v104, s[8:9]
	s_mov_b32 m0, s33
	s_ashr_i32 s13, s13, 6
	s_mov_b32 s20, 1
	s_cmp_lt_i32 s13, 1
	s_cbranch_scc1 .LBB2_7
	s_lshl_b64 s[8:9], s[10:11], 5
	s_cmp_lg_u32 0, -1
	s_cselect_b32 s33, 0, 0
	s_add_i32 s34, s33, s21
	s_add_i32 s33, s34, 0xa000
	s_add_i32 s34, s34, 0xe000
	s_lshl_b64 s[8:9], s[8:9], 1
	s_add_u32 s45, s4, s8
	s_addc_u32 s46, s5, s9
	s_add_u32 s43, s45, s14
	s_addc_u32 s44, s46, s15
	s_add_u32 s41, s43, s14
	s_addc_u32 s42, s44, s15
	s_add_u32 s35, s6, s8
	s_addc_u32 s38, s7, s9
	s_add_u32 s39, s35, s14
	s_addc_u32 s40, s38, s15
	s_add_u32 s47, s39, s14
	s_addc_u32 s48, s40, s15
	s_add_u32 s49, s47, s14
	s_addc_u32 s50, s48, s15
	s_add_u32 s51, s49, s14
	s_addc_u32 s52, s50, s15
	s_lshl_b64 s[36:37], s[10:11], 7
	s_sub_u32 s36, 0, s36
	s_subb_u32 s37, 0, s37
	s_add_u32 s61, s41, s36
	s_addc_u32 s62, s42, s37
	s_add_u32 s59, s61, s14
	s_addc_u32 s60, s62, s15
	s_add_u32 s57, s59, s14
	s_addc_u32 s58, s60, s15
	s_lshl_b64 s[10:11], s[10:11], 8
	s_sub_u32 s10, 0, s10
	s_subb_u32 s11, 0, s11
	s_add_u32 s53, s51, s10
	s_addc_u32 s54, s52, s11
	s_add_u32 s55, s53, s14
	s_addc_u32 s56, s54, s15
	s_add_u32 s63, s55, s14
	s_addc_u32 s64, s56, s15
	s_add_u32 s65, s63, s14
	s_addc_u32 s66, s64, s15
	s_add_u32 s67, s65, s14
	s_addc_u32 s68, s66, s15
	s_add_u32 s10, s35, 0x80
	s_addc_u32 s11, s38, 0
	s_add_u32 s14, s39, 0x80
	s_addc_u32 s15, s40, 0
	s_add_u32 s35, s47, 0x80
	s_addc_u32 s36, s48, 0
	s_add_u32 s37, s49, 0x80
	s_addc_u32 s38, s50, 0
	s_add_u32 s39, s51, 0x80
	s_addc_u32 s40, s52, 0
	s_add_u32 s41, s41, 0x80
	s_addc_u32 s42, s42, 0
	s_add_u32 s43, s43, 0x80
	s_addc_u32 s44, s44, 0
	s_add_u32 s45, s45, 0x80
	s_addc_u32 s46, s46, 0
	s_add_u32 s47, s53, 0x100
	s_addc_u32 s48, s54, 0
	s_add_u32 s49, s55, 0x100
	s_addc_u32 s50, s56, 0
	s_add_u32 s51, s63, 0x100
	s_addc_u32 s52, s64, 0
	s_add_u32 s53, s65, 0x100
	s_addc_u32 s54, s66, 0
	s_add_u32 s55, s67, 0x100
	s_addc_u32 s56, s68, 0
	v_and_b32_e32 v2, 15, v0
	v_bfe_u32 v0, v0, 1, 3
	s_add_u32 s57, s57, 0x100
	v_bitop3_b32 v0, v1, v0, 3 bitop3:0x6c
	s_addc_u32 s58, s58, 0
	v_lshlrev_b32_e32 v105, 4, v0
	v_or_b32_e32 v0, s18, v2
	s_add_u32 s59, s59, 0x100
	v_xor_b32_e32 v106, 64, v105
	v_lshl_add_u32 v0, v0, 7, 0
	s_addc_u32 s60, s60, 0
	v_or_b32_e32 v1, s16, v2
	v_add_u32_e32 v107, v0, v105
	v_add_u32_e32 v109, v0, v106
	s_add_u32 s61, s61, 0x100
	v_mov_b32_e32 v36, 0
	v_lshl_add_u32 v108, v1, 7, 0
	s_mov_b64 s[8:9], 0
	s_addc_u32 s62, s62, 0
	v_mov_b32_e32 v37, v36
	v_mov_b32_e32 v38, v36
	v_mov_b32_e32 v39, v36
	v_mov_b32_e32 v56, v36
	v_mov_b32_e32 v57, v36
	v_mov_b32_e32 v58, v36
	v_mov_b32_e32 v59, v36
	v_mov_b32_e32 v76, v36
	v_mov_b32_e32 v77, v36
	v_mov_b32_e32 v78, v36
	v_mov_b32_e32 v79, v36
	v_mov_b32_e32 v92, v36
	v_mov_b32_e32 v93, v36
	v_mov_b32_e32 v94, v36
	v_mov_b32_e32 v95, v36
	v_mov_b32_e32 v8, v36
	v_mov_b32_e32 v9, v36
	v_mov_b32_e32 v10, v36
	v_mov_b32_e32 v11, v36
	v_mov_b32_e32 v24, v36
	v_mov_b32_e32 v25, v36
	v_mov_b32_e32 v26, v36
	v_mov_b32_e32 v27, v36
	v_mov_b32_e32 v40, v36
	v_mov_b32_e32 v41, v36
	v_mov_b32_e32 v42, v36
	v_mov_b32_e32 v43, v36
	v_mov_b32_e32 v64, v36
	v_mov_b32_e32 v65, v36
	v_mov_b32_e32 v66, v36
	v_mov_b32_e32 v67, v36
	v_mov_b32_e32 v80, v36
	v_mov_b32_e32 v81, v36
	v_mov_b32_e32 v82, v36
	v_mov_b32_e32 v83, v36
	v_mov_b32_e32 v96, v36
	v_mov_b32_e32 v97, v36
	v_mov_b32_e32 v98, v36
	v_mov_b32_e32 v99, v36
	v_mov_b32_e32 v12, v36
	v_mov_b32_e32 v13, v36
	v_mov_b32_e32 v14, v36
	v_mov_b32_e32 v15, v36
	v_mov_b32_e32 v28, v36
	v_mov_b32_e32 v29, v36
	v_mov_b32_e32 v30, v36
	v_mov_b32_e32 v31, v36
	v_mov_b32_e32 v48, v36
	v_mov_b32_e32 v49, v36
	v_mov_b32_e32 v50, v36
	v_mov_b32_e32 v51, v36
	v_mov_b32_e32 v68, v36
	v_mov_b32_e32 v69, v36
	v_mov_b32_e32 v70, v36
	v_mov_b32_e32 v71, v36
	v_mov_b32_e32 v84, v36
	v_mov_b32_e32 v85, v36
	v_mov_b32_e32 v86, v36
	v_mov_b32_e32 v87, v36
	v_mov_b32_e32 v100, v36
	v_mov_b32_e32 v101, v36
	v_mov_b32_e32 v102, v36
	v_mov_b32_e32 v103, v36
	v_mov_b32_e32 v20, v36
	v_mov_b32_e32 v21, v36
	v_mov_b32_e32 v22, v36
	v_mov_b32_e32 v23, v36
	v_mov_b32_e32 v4, v36
	v_mov_b32_e32 v5, v36
	v_mov_b32_e32 v6, v36
	v_mov_b32_e32 v7, v36
	v_mov_b32_e32 v88, v36
	v_mov_b32_e32 v89, v36
	v_mov_b32_e32 v90, v36
	v_mov_b32_e32 v91, v36
	v_mov_b32_e32 v72, v36
	v_mov_b32_e32 v73, v36
	v_mov_b32_e32 v74, v36
	v_mov_b32_e32 v75, v36
	v_mov_b32_e32 v52, v36
	v_mov_b32_e32 v53, v36
	v_mov_b32_e32 v54, v36
	v_mov_b32_e32 v55, v36
	v_mov_b32_e32 v32, v36
	v_mov_b32_e32 v33, v36
	v_mov_b32_e32 v34, v36
	v_mov_b32_e32 v35, v36
	v_mov_b32_e32 v16, v36
	v_mov_b32_e32 v17, v36
	v_mov_b32_e32 v18, v36
	v_mov_b32_e32 v19, v36
	v_mov_b32_e32 v0, v36
	v_mov_b32_e32 v1, v36
	v_mov_b32_e32 v2, v36
	v_mov_b32_e32 v3, v36
	v_add_u32_e32 v110, 0x4000, v107
	v_add_u32_e32 v111, 0x4000, v109
	s_branch .LBB2_3
